# diff attention tile loop: K/V tile prefetch distance 2 (two register staging sets) on top of prologue hoist
# baseline (speedup 1.0000x reference)
; #define LAS __attribute__((address_space(3)))
; __device__ __forceinline__ int lt_tid(int wv) { int ln; asm volatile("v_mbcnt_lo_u32_b32 %0, -1, 0\n\tv_mbcnt_hi_u32_b32 %0, -1, %0" : "=v"(ln)); return (wv << 6) | ln; }
;     ...
;     const int tid = lt_tid(wvid), lane = tid & 63, wave = __builtin_amdgcn_readfirstlane(tid >> 6), l31 = lane & 31, hi = lane >> 5;
;     const bf16_t* U = (const bf16_t*)(ws + WS_U); const bf16_t* VT = (const bf16_t*)(ws + WS_VTD); bf16_t* MIX = (bf16_t*)(ws + WS_MIX);
;     unsigned* qhead = (unsigned*)(ws + WS_CTL) + CW_DQ + (qslot * 4 + l) * 64;
;     LAS float* btab = (LAS float*)lds;
;     LAS int* ucur = (LAS int*)(lds + 4 * 132 * 4);
;     LAS unsigned char* KV = lds + 4096;
;     constexpr float LOG2E = 1.4426950408889634f;
;     for (int i = tid; i < 4 * 129; i += NTHR) { const int h = i / 129, n = i % 129; btab[h * 132 + n] = p.in[I_RELB][t5_bucket(n) * 8 + 4 + h] * 5.656854249492381f; }
.LBB0_760:
	s_movk_i32 s32, 0x260
	s_mov_b32 s0, s65
	s_mov_b64 s[6:7], s[66:67]
	s_waitcnt vmcnt(1)
	v_mbcnt_lo_u32_b32 v32, -1, 0
	v_mbcnt_hi_u32_b32 v32, -1, v32
	s_movk_i32 s0, 0x204
	v_or_b32_e32 v30, s75, v32
	v_cmp_gt_i32_e32 vcc, s0, v30
	v_readfirstlane_b32 s20, v30
	s_and_saveexec_b64 s[0:1], vcc
	s_cbranch_execz .LBB0_765
	v_lshl_add_u32 v0, v30, 2, 0
	s_mov_b64 s[2:3], 0
	v_mov_b32_e32 v2, v30
	s_branch .LBB0_763

; #define LAS __attribute__((address_space(3)))
;     ...
;         const int qi = 16 - u / 32, bh = u % 32, b = bh >> 2, h = bh & 3;
;         const int q0 = qi == 0 ? 0 : 16 + 256 * (qi - 1), nkt = qi == 0 ? 1 : 4 * qi + 1;
;         const int q0w = q0 + 32 * wave, qpos = q0w + l31;
;         const bool wave_on = (qi > 0) || (wave == 0);
;         const size_t qrow = (size_t)b * LT + (qpos < LT ? qpos : LT - 1);
;         LAS bf16x8* Qs = (LAS bf16x8*)(lds + 4096 + 4 * DF_KB) + wave * 384 + lane;
;         const float farb = btab[h * 132 + 128] * c2;
;         float mref[2];
;         { const unsigned* kmx = (const unsigned*)(ws + WS_CTL) + CW_KMX + l * 256 + b * 8 + h * 2;
; #pragma unroll
;           for (int c = 0; c < 2; ++c) { float qn2 = 0.f;
; #pragma unroll
;               for (int s = 0; s < 2; ++s) { const u32x4 qv = *(const u32x4*)(U + qrow * INW + C_QD + h * 64 + c * 32 + s * 16 + hi * 8);
;                   const unsigned qw[4] = {qv.x, qv.y, qv.z, qv.w};
;                   { u32x4 qs; qs.x = pkbf(bflo(qw[0]) * c2, bfhi(qw[0]) * c2); qs.y = pkbf(bflo(qw[1]) * c2, bfhi(qw[1]) * c2); qs.z = pkbf(bflo(qw[2]) * c2, bfhi(qw[2]) * c2); qs.w = pkbf(bflo(qw[3]) * c2, bfhi(qw[3]) * c2);
;                     Qs[(c * 2 + s) * 64] = __builtin_bit_cast(bf16x8, qs); }
; #pragma unroll
;                   for (int e = 0; e < 4; ++e) qn2 += bflo(qw[e]) * bflo(qw[e]) + bfhi(qw[e]) * bfhi(qw[e]); }
;               qn2 += __shfl_xor(qn2, 32);
;               const float km2 = __uint_as_float(__hip_atomic_load(kmx + c, __ATOMIC_RELAXED, __HIP_MEMORY_SCOPE_AGENT));
;               mref[c] = (sqrtf(qn2 * km2) * 1.001f + btab[h * 132 + 129]) * c2;
;               { u32x4 qx; qx.x = hi ? 0u : (pkbf(farb - mref[c], 0.f) & 0xffffu); qx.y = 0u; qx.z = 0u; qx.w = 0u; Qs[(4 + c) * 64] = __builtin_bit_cast(bf16x8, qx); } } }
;         f32x16 O[2][2]; float lsum[2] = {0.f, 0.f};
; #pragma unroll
;         for (int c = 0; c < 2; ++c)
; #pragma unroll
;             for (int d = 0; d < 2; ++d)
; #pragma unroll
;                 for (int r = 0; r < 16; ++r) O[c][d][r] = 0.f;
;         const bf16_t* kbase = U + (size_t)b * LT * INW + C_KD + h * 64;
;         const bf16_t* vbase = VT + (size_t)bh * 64 * LTP;
;         const unsigned koff = (unsigned)(krow * INW + kch * 8), voff = (unsigned)(krow * LTP + kch * 8);
;         const float farraw = btab[h * 132 + 128];
.LBB0_774:
	s_or_b64 exec, exec, s[0:1]
	s_waitcnt lgkmcnt(0)
	s_barrier
	ds_read_b32 v0, v1 offset:2112
	s_movk_i32 s0, 0x21f
	s_waitcnt lgkmcnt(0)
	v_cmp_lt_i32_e32 vcc, s0, v0
	v_readfirstlane_b32 s30, v0
	s_mov_b64 s[0:1], -1
	s_cbranch_vccnz .LBB0_769
	s_ashr_i32 s0, s30, 31
	s_lshr_b32 s0, s0, 27
	s_add_i32 s0, s30, s0
	s_ashr_i32 s35, s0, 5
	s_andn2_b32 s0, s0, 31
	s_sub_i32 s34, s30, s0
	s_lshl_b32 s1, s35, 8
	s_sub_i32 s31, 16, s35
	s_ashr_i32 s0, s34, 2
	s_and_b32 s36, s34, 3
	s_sub_i32 s1, 0xf10, s1
	s_cmp_lg_u32 s31, 0
	s_cselect_b32 s49, s1, 0
	s_add_i32 s49, s49, s46
	s_mul_i32 s22, s0, 0x1010
	s_mul_i32 s1, s36, 0x210
	s_lshl_b32 s0, s0, 3
	v_add_u32_e32 v148, s49, v149
	s_add_i32 s50, s1, 0
	s_ashr_i32 s1, s0, 31
	s_ashr_i32 s23, s22, 31
	v_min_i32_e32 v2, 0x100f, v148
	s_lshl_b64 s[0:1], s[0:1], 2
	v_ashrrev_i32_e32 v3, 31, v2
	s_add_u32 s0, s47, s0
	v_lshl_add_u64 v[2:3], v[2:3], 0, s[22:23]
	s_addc_u32 s1, s48, s1
	s_lshl_b32 s28, s36, 3
	v_mov_b64_e32 v[4:5], s[8:9]
	s_add_u32 s24, s0, s28
	v_mad_u64_u32 v[4:5], s[38:39], v2, s97, v[4:5]
	s_addc_u32 s25, s1, 0
	v_mad_i32_i24 v5, v3, s97, v5
	s_lshl_b32 s40, s36, 7
	v_lshl_add_u64 v[2:3], v[4:5], 0, s[40:41]
	v_mov_b32_e32 v147, v1
	v_lshl_add_u64 v[4:5], v[2:3], 0, v[146:147]
	global_load_dwordx4 v[6:9], v[4:5], off offset:1024
	global_load_dwordx4 v[112:115], v[4:5], off offset:1056
	v_mov_b32_e32 v125, s28
	s_mul_i32 s58, s22, 0x1600
	global_load_dword v124, v125, s[0:1] sc1
	s_mul_hi_i32 s59, s22, 0x1600
	global_load_dwordx4 v[116:119], v[4:5], off offset:1088
	s_add_u32 s58, s8, s58
	s_addc_u32 s59, s9, s59
	global_load_dwordx4 v[120:123], v[4:5], off offset:1120
	s_lshl_b32 s60, s36, 7
	s_add_u32 s58, s58, s60
	s_addc_u32 s59, s59, 0
	global_load_dword v126, v1, s[24:25] offset:4 sc1
	s_mul_i32 s60, s34, 0x41000
	s_ashr_i32 s61, s60, 31
	s_lshl_b64 s[60:61], s[60:61], 1
	s_add_u32 s60, s42, s60
	s_addc_u32 s61, s43, s61
	v_lshl_add_u64 v[66:67], v[142:143], 1, s[58:59]
	v_lshl_add_u64 v[68:69], v[144:145], 1, s[60:61]
	global_load_dwordx4 v[102:105], v[66:67], off offset:1536
	global_load_dwordx4 v[106:109], v[68:69], off
	s_add_u32 s62, s58, 0x58000
	s_addc_u32 s63, s59, 0
	v_lshl_add_u64 v[70:71], v[142:143], 1, s[62:63]
	global_load_dwordx4 v[214:217], v[70:71], off offset:1536
	global_load_dwordx4 v[248:251], v[68:69], off offset:128
	v_mov_b32_e32 v0, s50
	ds_read_b32 v0, v0 offset:512
	v_and_b32_e32 v2, 64, v222
	v_add_u32_e32 v2, 64, v2
	s_waitcnt lgkmcnt(0)
	v_mul_f32_e32 v12, 0x3e8293ee, v0
	v_xor_b32_e32 v0, 32, v222
	v_cmp_lt_i32_e32 vcc, v0, v2
	s_waitcnt vmcnt(9)
	v_lshlrev_b32_e32 v2, 16, v6
	v_and_b32_e32 v3, 0xffff0000, v6
	v_pk_mul_f32 v[10:11], v[2:3], s[92:93] op_sel_hi:[1,0]
	v_pk_mul_f32 v[2:3], v[2:3], v[2:3]
	v_cvt_pk_bf16_f32 v6, v10, v11
	v_lshlrev_b32_e32 v10, 16, v7
	v_and_b32_e32 v11, 0xffff0000, v7
	v_pk_mul_f32 v[14:15], v[10:11], s[92:93] op_sel_hi:[1,0]
	v_add_f32_e32 v2, v2, v3
	v_cvt_pk_bf16_f32 v7, v14, v15
	v_lshlrev_b32_e32 v14, 16, v8
	v_and_b32_e32 v15, 0xffff0000, v8
	v_pk_mul_f32 v[16:17], v[14:15], s[92:93] op_sel_hi:[1,0]
	v_cndmask_b32_e32 v0, v222, v0, vcc
	v_cvt_pk_bf16_f32 v8, v16, v17
	v_lshlrev_b32_e32 v16, 16, v9
	v_and_b32_e32 v17, 0xffff0000, v9
	v_pk_mul_f32 v[18:19], v[16:17], s[92:93] op_sel_hi:[1,0]
	v_lshlrev_b32_e32 v190, 2, v0
	v_cvt_pk_bf16_f32 v9, v18, v19
	ds_write_b128 v189, v[6:9] offset:40960
	v_pk_mul_f32 v[8:9], v[10:11], v[10:11]
	v_pk_mul_f32 v[6:7], v[14:15], v[14:15]
	v_pk_mul_f32 v[10:11], v[16:17], v[16:17]
	v_add_f32_e32 v8, v8, v9
	v_add_f32_e32 v2, v2, v8
	v_add_f32_e32 v3, v6, v7
	v_add_f32_e32 v0, v10, v11
	v_add_f32_e32 v2, v3, v2
	v_add_f32_e32 v0, v0, v2
	s_waitcnt vmcnt(8)
	v_mov_b64_e32 v[14:15], v[112:113]
	v_mov_b64_e32 v[16:17], v[114:115]
	v_lshlrev_b32_e32 v18, 16, v14
	v_and_b32_e32 v19, 0xffff0000, v14
	v_pk_mul_f32 v[20:21], v[18:19], s[92:93] op_sel_hi:[1,0]
	s_nop 0
	v_cvt_pk_bf16_f32 v14, v20, v21
	v_lshlrev_b32_e32 v20, 16, v15
	v_and_b32_e32 v21, 0xffff0000, v15
	v_pk_mul_f32 v[22:23], v[20:21], s[92:93] op_sel_hi:[1,0]
	s_nop 0
	v_cvt_pk_bf16_f32 v15, v22, v23
	v_lshlrev_b32_e32 v22, 16, v16
	v_and_b32_e32 v23, 0xffff0000, v16
	v_pk_mul_f32 v[24:25], v[22:23], s[92:93] op_sel_hi:[1,0]
	s_nop 0
	v_cvt_pk_bf16_f32 v16, v24, v25
	v_lshlrev_b32_e32 v24, 16, v17
	v_and_b32_e32 v25, 0xffff0000, v17
	v_pk_mul_f32 v[26:27], v[24:25], s[92:93] op_sel_hi:[1,0]
	s_nop 0
	v_cvt_pk_bf16_f32 v17, v26, v27
	ds_write_b128 v189, v[14:17] offset:41984
	v_pk_mul_f32 v[14:15], v[18:19], v[18:19]
	v_pk_mul_f32 v[16:17], v[20:21], v[20:21]
	v_add_f32_e32 v2, v14, v15
	v_pk_mul_f32 v[18:19], v[22:23], v[22:23]
	v_add_f32_e32 v0, v2, v0
	v_add_f32_e32 v2, v16, v17
	v_pk_mul_f32 v[20:21], v[24:25], v[24:25]
	v_add_f32_e32 v0, v2, v0
	v_add_f32_e32 v2, v18, v19
	v_add_f32_e32 v0, v2, v0
	v_add_f32_e32 v2, v20, v21
	v_add_f32_e32 v2, v2, v0
	v_mov_b32_e32 v0, s28
	ds_bpermute_b32 v3, v190, v2
	v_mov_b32_e32 v18, 0
	v_mov_b32_e32 v0, 0
	s_and_saveexec_b64 s[28:29], s[4:5]
	s_cbranch_execz .LBB0_777
	s_waitcnt lgkmcnt(0)
	v_add_f32_e32 v0, v2, v3
	s_waitcnt vmcnt(7)
	v_mul_f32_e32 v0, v0, v124
	s_mov_b32 s0, 0xf800000
	v_mul_f32_e32 v2, 0x4f800000, v0
	v_cmp_gt_f32_e32 vcc, s0, v0
	s_nop 1
	v_cndmask_b32_e32 v0, v0, v2, vcc
	v_sqrt_f32_e32 v2, v0
	s_nop 0
	v_add_u32_e32 v3, -1, v2
	v_fma_f32 v7, -v3, v2, v0
	v_add_u32_e32 v6, 1, v2
	v_cmp_ge_f32_e64 s[0:1], 0, v7
	s_nop 1
	v_cndmask_b32_e64 v3, v2, v3, s[0:1]
	v_fma_f32 v2, -v6, v2, v0
	v_cmp_lt_f32_e64 s[0:1], 0, v2
	s_nop 1
	v_cndmask_b32_e64 v2, v3, v6, s[0:1]
	v_mov_b32_e32 v3, s50
	ds_read_b32 v3, v3 offset:516
	v_mul_f32_e32 v6, 0x37800000, v2
	v_cndmask_b32_e32 v2, v2, v6, vcc
	v_cmp_class_f32_e64 vcc, v0, s32
	s_nop 1
	v_cndmask_b32_e32 v0, v2, v0, vcc
	s_waitcnt lgkmcnt(0)
	v_fmac_f32_e32 v3, 0x3f8020c5, v0
	v_fmamk_f32 v0, v3, 0xbe8293ee, v12
	v_cvt_pk_bf16_f32 v0, v0, 0
	v_and_b32_e32 v0, 0xffff, v0
; #define LAS __attribute__((address_space(3)))
; __device__ __forceinline__ float bflo(unsigned w) { return __uint_as_float(w << 16); }
; __device__ __forceinline__ float bfhi(unsigned w) { return __uint_as_float(w & 0xFFFF0000u); }
; __device__ __forceinline__ unsigned pkbf(float lo, float hi) { f32x2_t v = {lo, hi}; bf16x2_t b = __builtin_convertvector(v, bf16x2_t); return __builtin_bit_cast(unsigned, b); }
;     ...
;               for (int s = 0; s < 2; ++s) { const u32x4 qv = *(const u32x4*)(U + qrow * INW + C_QD + h * 64 + c * 32 + s * 16 + hi * 8);
;                   const unsigned qw[4] = {qv.x, qv.y, qv.z, qv.w};
;                   { u32x4 qs; qs.x = pkbf(bflo(qw[0]) * c2, bfhi(qw[0]) * c2); qs.y = pkbf(bflo(qw[1]) * c2, bfhi(qw[1]) * c2); qs.z = pkbf(bflo(qw[2]) * c2, bfhi(qw[2]) * c2); qs.w = pkbf(bflo(qw[3]) * c2, bfhi(qw[3]) * c2);
;                     Qs[(c * 2 + s) * 64] = __builtin_bit_cast(bf16x8, qs); }
; #pragma unroll
;                   for (int e = 0; e < 4; ++e) qn2 += bflo(qw[e]) * bflo(qw[e]) + bfhi(qw[e]) * bfhi(qw[e]); }
;               qn2 += __shfl_xor(qn2, 32);
;               const float km2 = __uint_as_float(__hip_atomic_load(kmx + c, __ATOMIC_RELAXED, __HIP_MEMORY_SCOPE_AGENT));
;               mref[c] = (sqrtf(qn2 * km2) * 1.001f + btab[h * 132 + 129]) * c2;
;               { u32x4 qx; qx.x = hi ? 0u : (pkbf(farb - mref[c], 0.f) & 0xffffu); qx.y = 0u; qx.z = 0u; qx.w = 0u; Qs[(4 + c) * 64] = __builtin_bit_cast(bf16x8, qx); } } }
;         f32x16 O[2][2]; float lsum[2] = {0.f, 0.f};
; #pragma unroll
;         for (int c = 0; c < 2; ++c)
; #pragma unroll
;             for (int d = 0; d < 2; ++d)
; #pragma unroll
;                 for (int r = 0; r < 16; ++r) O[c][d][r] = 0.f;
;         const bf16_t* kbase = U + (size_t)b * LT * INW + C_KD + h * 64;
;         const bf16_t* vbase = VT + (size_t)bh * 64 * LTP;
;         const unsigned koff = (unsigned)(krow * INW + kch * 8), voff = (unsigned)(krow * LTP + kch * 8);
;         const float farraw = btab[h * 132 + 128];
;         u32x4 kreg = *(const u32x4*)(kbase + koff), vreg = *(const u32x4*)(vbase + voff);
;         *(LAS u32x4*)(KV + krow * DF_PITCH + kch * 16) = kreg; *(LAS u32x4*)(KV + 2 * DF_KB + krow * DF_PITCH + kch * 16) = vreg;
;         __syncthreads();
.LBB0_777:
	s_or_b64 exec, exec, s[28:29]
	v_mov_b32_e32 v2, v1
	s_waitcnt lgkmcnt(0)
	v_mov_b32_e32 v3, v1
	ds_write_b128 v189, v[0:3] offset:45056
	s_mov_b32 s51, 0
	s_waitcnt vmcnt(6)
	v_mov_b64_e32 v[6:7], v[116:117]
	v_mov_b64_e32 v[8:9], v[118:119]
	v_lshlrev_b32_e32 v2, 16, v6
	v_and_b32_e32 v3, 0xffff0000, v6
	v_pk_mul_f32 v[10:11], v[2:3], s[92:93] op_sel_hi:[1,0]
	v_pk_mul_f32 v[2:3], v[2:3], v[2:3]
	v_cvt_pk_bf16_f32 v6, v10, v11
	v_lshlrev_b32_e32 v10, 16, v7
	v_and_b32_e32 v11, 0xffff0000, v7
	v_pk_mul_f32 v[14:15], v[10:11], s[92:93] op_sel_hi:[1,0]
	v_add_f32_e32 v2, v2, v3
	v_cvt_pk_bf16_f32 v7, v14, v15
	v_lshlrev_b32_e32 v14, 16, v8
	v_and_b32_e32 v15, 0xffff0000, v8
	v_pk_mul_f32 v[16:17], v[14:15], s[92:93] op_sel_hi:[1,0]
	s_nop 0
	v_cvt_pk_bf16_f32 v8, v16, v17
	v_lshlrev_b32_e32 v16, 16, v9
	v_and_b32_e32 v17, 0xffff0000, v9
	v_pk_mul_f32 v[20:21], v[16:17], s[92:93] op_sel_hi:[1,0]
	s_nop 0
	v_cvt_pk_bf16_f32 v9, v20, v21
	ds_write_b128 v189, v[6:9] offset:43008
	v_pk_mul_f32 v[8:9], v[10:11], v[10:11]
	v_pk_mul_f32 v[6:7], v[14:15], v[14:15]
	v_pk_mul_f32 v[10:11], v[16:17], v[16:17]
	v_add_f32_e32 v8, v8, v9
	v_add_f32_e32 v2, v2, v8
	v_add_f32_e32 v3, v6, v7
	v_add_f32_e32 v2, v3, v2
	v_add_f32_e32 v0, v10, v11
	v_add_f32_e32 v0, v0, v2
	s_waitcnt vmcnt(5)
	v_mov_b64_e32 v[14:15], v[120:121]
	v_mov_b64_e32 v[16:17], v[122:123]
	v_lshlrev_b32_e32 v4, 16, v14
	v_and_b32_e32 v5, 0xffff0000, v14
	v_pk_mul_f32 v[20:21], v[4:5], s[92:93] op_sel_hi:[1,0]
	v_pk_mul_f32 v[4:5], v[4:5], v[4:5]
	v_cvt_pk_bf16_f32 v14, v20, v21
	v_lshlrev_b32_e32 v20, 16, v15
	v_and_b32_e32 v21, 0xffff0000, v15
	v_pk_mul_f32 v[22:23], v[20:21], s[92:93] op_sel_hi:[1,0]
	v_add_f32_e32 v2, v4, v5
	v_cvt_pk_bf16_f32 v15, v22, v23
	v_lshlrev_b32_e32 v22, 16, v16
	v_and_b32_e32 v23, 0xffff0000, v16
	v_pk_mul_f32 v[24:25], v[22:23], s[92:93] op_sel_hi:[1,0]
	v_add_f32_e32 v0, v2, v0
	v_cvt_pk_bf16_f32 v16, v24, v25
	v_lshlrev_b32_e32 v24, 16, v17
	v_and_b32_e32 v25, 0xffff0000, v17
	v_pk_mul_f32 v[26:27], v[24:25], s[92:93] op_sel_hi:[1,0]
	s_nop 0
	v_cvt_pk_bf16_f32 v17, v26, v27
	ds_write_b128 v189, v[14:17] offset:44032
	v_pk_mul_f32 v[14:15], v[20:21], v[20:21]
	v_pk_mul_f32 v[16:17], v[22:23], v[22:23]
	v_add_f32_e32 v2, v14, v15
	v_pk_mul_f32 v[20:21], v[24:25], v[24:25]
	v_add_f32_e32 v0, v2, v0
	v_add_f32_e32 v2, v16, v17
	v_add_f32_e32 v0, v2, v0
	v_add_f32_e32 v2, v20, v21
	v_add_f32_e32 v0, v2, v0
	ds_bpermute_b32 v2, v190, v0
	s_and_saveexec_b64 s[24:25], s[4:5]
	s_cbranch_execz .LBB0_779
	s_waitcnt lgkmcnt(0)
	v_add_f32_e32 v0, v0, v2
	s_waitcnt vmcnt(4)
	v_mul_f32_e32 v0, v0, v126
	s_mov_b32 s0, 0xf800000
	v_mul_f32_e32 v2, 0x4f800000, v0
	v_cmp_gt_f32_e32 vcc, s0, v0
	s_nop 1
	v_cndmask_b32_e32 v0, v0, v2, vcc
	v_sqrt_f32_e32 v2, v0
	s_nop 0
	v_add_u32_e32 v3, -1, v2
	v_fma_f32 v5, -v3, v2, v0
	v_add_u32_e32 v4, 1, v2
	v_cmp_ge_f32_e64 s[0:1], 0, v5
	s_nop 1
	v_cndmask_b32_e64 v3, v2, v3, s[0:1]
	v_fma_f32 v2, -v4, v2, v0
	v_cmp_lt_f32_e64 s[0:1], 0, v2
	s_nop 1
	v_cndmask_b32_e64 v2, v3, v4, s[0:1]
	v_mov_b32_e32 v3, s50
	ds_read_b32 v3, v3 offset:516
	v_mul_f32_e32 v4, 0x37800000, v2
	v_cndmask_b32_e32 v2, v2, v4, vcc
	v_cmp_class_f32_e64 vcc, v0, s32
	s_nop 1
	v_cndmask_b32_e32 v0, v2, v0, vcc
	s_waitcnt lgkmcnt(0)
	v_fmac_f32_e32 v3, 0x3f8020c5, v0
	v_fmac_f32_e32 v12, 0xbe8293ee, v3
	v_cvt_pk_bf16_f32 v0, v12, 0
	v_and_b32_e32 v18, 0xffff, v0
.LBB0_779:
	s_or_b64 exec, exec, s[24:25]
	s_sub_i32 s37, 0, s35
	s_lshl_b32 s0, s36, 6
	s_cmpk_lt_i32 s30, 0x200
	s_cselect_b64 s[24:25], -1, 0
	s_lshl_b32 s52, s31, 2
	s_or_b64 s[28:29], s[24:25], s[18:19]
	s_mul_i32 s30, s22, 0x1600
	s_mul_hi_i32 s1, s22, 0x1600
	s_add_u32 s30, s8, s30
	s_addc_u32 s1, s9, s1
	s_lshl_b32 s40, s0, 1
	s_add_u32 s30, s30, s40
	s_mul_i32 s0, s34, 0x41000
	s_addc_u32 s31, s1, 0
	s_ashr_i32 s1, s0, 31
	s_lshl_b64 s[0:1], s[0:1], 1
	s_add_u32 s34, s42, s0
	s_addc_u32 s35, s43, s1
	s_waitcnt vmcnt(4) lgkmcnt(0)
	v_lshl_add_u64 v[2:3], v[142:143], 1, s[30:31]
	v_lshl_add_u64 v[4:5], v[144:145], 1, s[34:35]
	v_mov_b32_e32 v19, v1
	v_mov_b32_e32 v20, v1
	v_mov_b32_e32 v21, v1
	v_mov_b32_e32 v22, s50
	ds_write_b128 v189, v[18:21] offset:46080
	ds_read_b32 v150, v22 offset:512
	v_mov_b32_e32 v16, v1
	v_mov_b32_e32 v17, v1
	v_mov_b32_e32 v2, v1
	v_mov_b32_e32 v3, v1
	v_mov_b32_e32 v4, v1
	v_mov_b32_e32 v5, v1
	v_mov_b32_e32 v6, v1
	v_mov_b32_e32 v7, v1
	v_mov_b32_e32 v8, v1
	v_mov_b32_e32 v9, v1
	v_mov_b32_e32 v10, v1
	v_mov_b32_e32 v11, v1
	v_mov_b32_e32 v12, v1
	v_mov_b32_e32 v13, v1
	v_mov_b32_e32 v14, v1
	v_mov_b32_e32 v15, v1
	v_mov_b64_e32 v[48:49], v[16:17]
	v_mov_b64_e32 v[32:33], v[16:17]
	v_mov_b64_e32 v[64:65], v[16:17]
	s_lshl_b32 s55, s37, 2
	v_mov_b32_e32 v147, v148
	v_mov_b32_e32 v191, 0
	v_add_u32_e32 v0, 0x58000, v142
	v_mov_b32_e32 v192, 0
	v_mov_b64_e32 v[46:47], v[14:15]
	v_mov_b64_e32 v[44:45], v[12:13]
	v_mov_b64_e32 v[42:43], v[10:11]
	v_mov_b64_e32 v[40:41], v[8:9]
	v_mov_b64_e32 v[38:39], v[6:7]
	v_mov_b64_e32 v[36:37], v[4:5]
	v_mov_b64_e32 v[34:35], v[2:3]
	v_mov_b64_e32 v[30:31], v[14:15]
	v_mov_b64_e32 v[28:29], v[12:13]
	v_mov_b64_e32 v[26:27], v[10:11]
	v_mov_b64_e32 v[24:25], v[8:9]
	v_mov_b64_e32 v[22:23], v[6:7]
	v_mov_b64_e32 v[20:21], v[4:5]
	v_mov_b64_e32 v[18:19], v[2:3]
	v_mov_b64_e32 v[62:63], v[14:15]
	v_mov_b64_e32 v[60:61], v[12:13]
	v_mov_b64_e32 v[58:59], v[10:11]
	v_mov_b64_e32 v[56:57], v[8:9]
	v_mov_b64_e32 v[54:55], v[6:7]
	v_mov_b64_e32 v[52:53], v[4:5]
	v_mov_b64_e32 v[50:51], v[2:3]
	s_waitcnt lgkmcnt(0)
	v_mov_b32_e32 v151, v150
	s_add_i32 s53, s49, 31
	s_sub_i32 s54, s49, 63
	s_addk_i32 s55, 0x41
	s_mov_b32 s56, 0
	s_waitcnt vmcnt(3)
	ds_write_b128 v185, v[102:105] offset:4096
	s_waitcnt vmcnt(2)
	ds_write_b128 v185, v[106:109] offset:22528
	s_waitcnt lgkmcnt(0)
	s_barrier
	s_branch .LBB0_781

;     ...
;         for (int kt = 0; kt < nkt; ++kt) {
;             const int k0 = kt * 64, cur = kt & 1;
;             if (kt + 1 < nkt) { kreg = *(const u32x4*)(kbase + (koff + (unsigned)((k0 + 64) * INW))); vreg = *(const u32x4*)(vbase + (voff + (unsigned)(k0 + 64))); }
.LBB0_781:
	s_cmp_lt_u32 s56, s52
	s_cselect_b64 s[36:37], -1, 0
	s_add_i32 s58, s56, 1
	s_cmp_ge_u32 s58, s52
	s_cselect_b32 s59, 0, 2
	s_cbranch_scc1 .LBB0_783
	v_add_u32_e32 v68, 0x80, v144
	v_lshl_add_u64 v[66:67], v[0:1], 1, s[30:31]
	v_add_u32_e32 v68, s51, v68
	v_mov_b32_e32 v69, v1
	v_lshl_add_u64 v[68:69], v[68:69], 1, s[34:35]
	s_bitcmp1_b32 s56, 0
	s_cbranch_scc1 .Ldf_ldB
	global_load_dwordx4 v[102:105], v[66:67], off offset:1536
	global_load_dwordx4 v[106:109], v[68:69], off
	s_branch .LBB0_783
.Ldf_ldB:
	global_load_dwordx4 v[214:217], v[66:67], off offset:1536
	global_load_dwordx4 v[248:251], v[68:69], off

; #define LAS __attribute__((address_space(3)))
; __device__ __forceinline__ void diff_tile(const bool near, const LAS unsigned char* Kb, const LAS unsigned char* Vb, const LAS float* btab, const LAS bf16x8* Qs, f32x16 (&O)[2][2],
;                                           float (&lsum)[2], int qpos, int k0, int l31, int hi, float c2, float farraw) {
;     ...
;             for (int s = 0; s < 2; ++s) { const bf16x8 kf = *(const LAS bf16x8*)(Kb + (32 * kb + l31) * DF_PITCH + c * 64 + s * 32 + hi * 16);
;                 acc = __builtin_amdgcn_mfma_f32_32x32x16_bf16(kf, Qs[(c * 2 + s) * 64], acc, 0, 0, 0); }
;             acc = __builtin_amdgcn_mfma_f32_32x32x16_bf16(kx, Qs[(4 + c) * 64], acc, 0, 0, 0);
;             S[kb] = acc;
;         }
;         if (near) {
; #pragma unroll
;             for (int kb = 0; kb < 2; ++kb)
; #pragma unroll
;                 for (int r = 0; r < 16; ++r) S[kb][r] += bm[kb][r]; }
;         float ls = 0.f;
;         bf16x8 Pf[4];
; #pragma unroll
;         for (int kb = 0; kb < 2; ++kb) {
; #pragma unroll
;             for (int r = 0; r < 16; ++r) { const float pv = __builtin_amdgcn_exp2f(S[kb][r]); ls += pv; S[kb][r] = pv; }
; #pragma unroll
;             for (int s = 0; s < 2; ++s) Pf[2 * kb + s] = pack_acc(S[kb], s);
;         }
;         lsum[c] += ls;
; #pragma unroll
;         for (int st = 0; st < 4; ++st)
; #pragma unroll
;             for (int dvb = 0; dvb < 2; ++dvb) O[c][dvb] = __builtin_amdgcn_mfma_f32_32x32x16_bf16(Vf[st][dvb], Pf[st], O[c][dvb], 0, 0, 0);
.LBB0_788:
	s_nop 9
	v_exp_f32_e32 v194, v82
	v_exp_f32_e32 v195, v83
	v_exp_f32_e32 v196, v84
	v_exp_f32_e32 v197, v85
	v_exp_f32_e32 v198, v86
	v_exp_f32_e32 v199, v87
	v_exp_f32_e32 v223, v88
	v_exp_f32_e32 v224, v89
	v_cvt_pk_bf16_f32 v82, v194, v195
	v_cvt_pk_bf16_f32 v83, v196, v197
	v_cvt_pk_bf16_f32 v84, v198, v199
	v_cvt_pk_bf16_f32 v85, v223, v224
	v_exp_f32_e32 v225, v90
	v_exp_f32_e32 v226, v91
	s_waitcnt lgkmcnt(7)
	v_mfma_f32_32x32x16_bf16 v[50:65], v[138:141], v[82:85], v[50:65]
	v_exp_f32_e32 v227, v92
	v_exp_f32_e32 v228, v93
	v_exp_f32_e32 v229, v94
	v_exp_f32_e32 v230, v95
	v_exp_f32_e32 v231, v96
	v_exp_f32_e32 v232, v97
	v_exp_f32_e32 v233, v66
	s_waitcnt lgkmcnt(2)
	v_mfma_f32_32x32x16_bf16 v[18:33], v[134:137], v[82:85], v[18:33]
	v_cvt_pk_bf16_f32 v82, v225, v226
	v_cvt_pk_bf16_f32 v83, v227, v228
	v_cvt_pk_bf16_f32 v84, v229, v230
	v_cvt_pk_bf16_f32 v85, v231, v232
	v_exp_f32_e32 v234, v67
	v_exp_f32_e32 v235, v68
	v_exp_f32_e32 v236, v69
	v_mfma_f32_32x32x16_bf16 v[50:65], v[130:133], v[82:85], v[50:65]
	v_exp_f32_e32 v237, v70
	v_exp_f32_e32 v238, v71
	v_exp_f32_e32 v239, v72
	v_exp_f32_e32 v240, v73
	v_cvt_pk_bf16_f32 v66, v233, v234
	v_cvt_pk_bf16_f32 v67, v235, v236
	v_cvt_pk_bf16_f32 v68, v237, v238
	v_mfma_f32_32x32x16_bf16 v[18:33], v[126:129], v[82:85], v[18:33]
	v_cvt_pk_bf16_f32 v69, v239, v240
	v_exp_f32_e32 v241, v74
	v_exp_f32_e32 v242, v75
	v_exp_f32_e32 v243, v76
	v_exp_f32_e32 v244, v77
	v_exp_f32_e32 v245, v78
	v_exp_f32_e32 v246, v79
	v_mfma_f32_32x32x16_bf16 v[50:65], v[122:125], v[66:69], v[50:65]
	v_exp_f32_e32 v247, v80
	v_exp_f32_e32 v205, v81
	s_and_b64 vcc, exec, s[0:1]
	v_mfma_f32_32x32x16_bf16 v[18:33], v[118:121], v[66:69], v[18:33]
	v_cvt_pk_bf16_f32 v66, v241, v242
	v_cvt_pk_bf16_f32 v67, v243, v244
	v_cvt_pk_bf16_f32 v68, v245, v246
	v_cvt_pk_bf16_f32 v69, v247, v205
	s_waitcnt lgkmcnt(1)
	s_nop 0
	v_mfma_f32_32x32x16_bf16 v[50:65], v[114:117], v[66:69], v[50:65]
	s_waitcnt lgkmcnt(0)
	v_mfma_f32_32x32x16_bf16 v[18:33], v[110:113], v[66:69], v[18:33]
	ds_read_b128 v[66:69], v193 offset:4160
	ds_read_b128 v[70:73], v189 offset:43008
	ds_read_b128 v[206:209], v189 offset:44032
	ds_read_b128 v[210:213], v189 offset:46080
	s_waitcnt lgkmcnt(2)
	v_mfma_f32_32x32x16_bf16 v[82:97], v[66:69], v[70:73], 0
	ds_read_b128 v[66:69], v193 offset:4192
	ds_read_b128 v[74:77], v193 offset:8768
	ds_read_b128 v[200:203], v193 offset:8800
	s_waitcnt lgkmcnt(2)
	v_mfma_f32_32x32x16_bf16 v[82:97], v[66:69], v[206:209], v[82:97]
	s_waitcnt lgkmcnt(1)
	v_mfma_f32_32x32x16_bf16 v[66:81], v[74:77], v[70:73], 0
	s_waitcnt lgkmcnt(0)
	v_mfma_f32_32x32x16_bf16 v[66:81], v[200:203], v[206:209], v[66:81]
	v_mfma_f32_32x32x16_bf16 v[82:97], v[98:101], v[210:213], v[82:97]
	v_mfma_f32_32x32x16_bf16 v[66:81], v[98:101], v[210:213], v[66:81]
	s_cbranch_vccnz .LBB0_790
	s_nop 9
	v_pk_add_f32 v[82:83], v[152:153], v[82:83]
	v_pk_add_f32 v[84:85], v[154:155], v[84:85]
	v_pk_add_f32 v[86:87], v[156:157], v[86:87]
	v_pk_add_f32 v[88:89], v[158:159], v[88:89]
	v_pk_add_f32 v[90:91], v[160:161], v[90:91]
	v_pk_add_f32 v[92:93], v[162:163], v[92:93]
	v_pk_add_f32 v[94:95], v[164:165], v[94:95]
	v_pk_add_f32 v[96:97], v[166:167], v[96:97]
	v_pk_add_f32 v[66:67], v[168:169], v[66:67]
	v_pk_add_f32 v[68:69], v[170:171], v[68:69]
	v_pk_add_f32 v[70:71], v[172:173], v[70:71]
	v_pk_add_f32 v[72:73], v[174:175], v[72:73]
	v_pk_add_f32 v[74:75], v[176:177], v[74:75]
	v_pk_add_f32 v[76:77], v[178:179], v[76:77]
	v_pk_add_f32 v[78:79], v[180:181], v[78:79]
	v_pk_add_f32 v[80:81], v[182:183], v[80:81]
; #define LAS __attribute__((address_space(3)))
; __device__ __forceinline__ void diff_tile(const bool near, const LAS unsigned char* Kb, const LAS unsigned char* Vb, const LAS float* btab, const LAS bf16x8* Qs, f32x16 (&O)[2][2],
;                                           float (&lsum)[2], int qpos, int k0, int l31, int hi, float c2, float farraw) {
;     ...
;         float ls = 0.f;
;         bf16x8 Pf[4];
; #pragma unroll
;         for (int kb = 0; kb < 2; ++kb) {
; #pragma unroll
;             for (int r = 0; r < 16; ++r) { const float pv = __builtin_amdgcn_exp2f(S[kb][r]); ls += pv; S[kb][r] = pv; }
; #pragma unroll
;             for (int s = 0; s < 2; ++s) Pf[2 * kb + s] = pack_acc(S[kb], s);
;         }
;         lsum[c] += ls;
; #pragma unroll
;         for (int st = 0; st < 4; ++st)
; #pragma unroll
;             for (int dvb = 0; dvb < 2; ++dvb) O[c][dvb] = __builtin_amdgcn_mfma_f32_32x32x16_bf16(Vf[st][dvb], Pf[st], O[c][dvb], 0, 0, 0);
;     }
;     ...
;             if (kt + 1 < nkt) { *(LAS u32x4*)(KV + (cur ^ 1) * DF_KB + krow * DF_PITCH + kch * 16) = kreg; *(LAS u32x4*)(KV + (2 + (cur ^ 1)) * DF_KB + krow * DF_PITCH + kch * 16) = vreg; }
;             __syncthreads();
.LBB0_790:
	v_add_f32_e32 v152, 0, v194
	v_add_f32_e32 v152, v195, v152
	v_add_f32_e32 v152, v196, v152
	v_add_f32_e32 v152, v197, v152
	v_add_f32_e32 v152, v198, v152
	v_add_f32_e32 v152, v199, v152
	v_add_f32_e32 v152, v223, v152
	v_add_f32_e32 v152, v224, v152
	v_add_f32_e32 v152, v225, v152
	v_add_f32_e32 v152, v226, v152
	v_add_f32_e32 v152, v227, v152
	v_add_f32_e32 v152, v228, v152
	v_add_f32_e32 v152, v229, v152
	v_add_f32_e32 v152, v230, v152
	v_add_f32_e32 v152, v231, v152
	v_add_f32_e32 v152, v232, v152
	v_add_f32_e32 v152, v233, v152
	v_add_f32_e32 v152, v234, v152
	v_add_f32_e32 v152, v235, v152
	v_add_f32_e32 v152, v236, v152
	v_add_f32_e32 v152, v237, v152
	v_add_f32_e32 v152, v238, v152
	v_add_f32_e32 v152, v239, v152
	v_add_f32_e32 v152, v240, v152
	v_add_f32_e32 v152, v241, v152
	v_add_f32_e32 v152, v242, v152
	v_add_f32_e32 v152, v243, v152
	v_add_f32_e32 v152, v244, v152
	v_add_f32_e32 v152, v245, v152
	v_add_f32_e32 v152, v246, v152
	v_add_f32_e32 v152, v247, v152
	v_add_f32_e32 v152, v205, v152
	v_add_f32_e32 v191, v191, v152
	v_exp_f32_e32 v152, v82
	v_exp_f32_e32 v153, v83
	v_exp_f32_e32 v154, v84
	v_exp_f32_e32 v155, v85
	v_exp_f32_e32 v156, v86
	v_exp_f32_e32 v157, v87
	v_exp_f32_e32 v158, v88
	v_exp_f32_e32 v159, v89
	v_cvt_pk_bf16_f32 v82, v152, v153
	v_add_f32_e32 v152, 0, v152
	v_add_f32_e32 v152, v153, v152
	v_add_f32_e32 v152, v154, v152
	v_cvt_pk_bf16_f32 v83, v154, v155
	v_cvt_pk_bf16_f32 v84, v156, v157
	v_cvt_pk_bf16_f32 v85, v158, v159
	v_add_f32_e32 v152, v155, v152
	v_exp_f32_e32 v90, v90
	v_exp_f32_e32 v91, v91
	v_add_f32_e32 v152, v156, v152
	v_mfma_f32_32x32x16_bf16 v[34:49], v[138:141], v[82:85], v[34:49]
	v_add_f32_e32 v152, v157, v152
	v_exp_f32_e32 v92, v92
	v_add_f32_e32 v152, v158, v152
	v_exp_f32_e32 v93, v93
	v_exp_f32_e32 v94, v94
	v_exp_f32_e32 v95, v95
	v_exp_f32_e32 v96, v96
	v_mfma_f32_32x32x16_bf16 v[2:17], v[134:137], v[82:85], v[2:17]
	v_exp_f32_e32 v97, v97
	v_add_f32_e32 v152, v159, v152
	v_cvt_pk_bf16_f32 v86, v90, v91
	v_add_f32_e32 v90, v90, v152
	v_add_f32_e32 v90, v91, v90
	v_add_f32_e32 v90, v92, v90
	v_cvt_pk_bf16_f32 v87, v92, v93
	v_cvt_pk_bf16_f32 v88, v94, v95
	v_cvt_pk_bf16_f32 v89, v96, v97
	v_add_f32_e32 v90, v93, v90
	v_add_f32_e32 v90, v94, v90
	v_mfma_f32_32x32x16_bf16 v[34:49], v[130:133], v[86:89], v[34:49]
	v_add_f32_e32 v90, v95, v90
	v_add_f32_e32 v90, v96, v90
	v_add_f32_e32 v82, v97, v90
	v_exp_f32_e32 v83, v66
	v_exp_f32_e32 v84, v67
	v_exp_f32_e32 v85, v68
	v_exp_f32_e32 v90, v69
	v_mfma_f32_32x32x16_bf16 v[2:17], v[126:129], v[86:89], v[2:17]
	v_exp_f32_e32 v91, v70
	v_exp_f32_e32 v92, v71
	v_exp_f32_e32 v93, v72
	v_exp_f32_e32 v94, v73
	v_cvt_pk_bf16_f32 v66, v83, v84
	v_cvt_pk_bf16_f32 v67, v85, v90
	v_cvt_pk_bf16_f32 v68, v91, v92
	v_cvt_pk_bf16_f32 v69, v93, v94
	v_add_f32_e32 v82, v83, v82
	v_add_f32_e32 v82, v84, v82
	v_mfma_f32_32x32x16_bf16 v[34:49], v[122:125], v[66:69], v[34:49]
	v_add_f32_e32 v82, v85, v82
	v_exp_f32_e32 v74, v74
	v_exp_f32_e32 v75, v75
	v_exp_f32_e32 v76, v76
	v_exp_f32_e32 v77, v77
	v_exp_f32_e32 v78, v78
	v_exp_f32_e32 v79, v79
	v_mfma_f32_32x32x16_bf16 v[2:17], v[118:121], v[66:69], v[2:17]
	v_add_f32_e32 v66, v90, v82
	v_exp_f32_e32 v80, v80
	v_exp_f32_e32 v81, v81
	v_add_f32_e32 v66, v91, v66
	v_add_f32_e32 v66, v92, v66
	v_add_f32_e32 v66, v93, v66
	v_add_f32_e32 v66, v94, v66
	v_cvt_pk_bf16_f32 v70, v74, v75
	v_cvt_pk_bf16_f32 v71, v76, v77
	v_cvt_pk_bf16_f32 v72, v78, v79
	v_cvt_pk_bf16_f32 v73, v80, v81
	v_add_f32_e32 v66, v74, v66
	v_add_f32_e32 v66, v75, v66
	v_mfma_f32_32x32x16_bf16 v[34:49], v[114:117], v[70:73], v[34:49]
	v_add_f32_e32 v66, v76, v66
	v_add_f32_e32 v66, v77, v66
	v_add_f32_e32 v66, v78, v66
	v_add_f32_e32 v66, v79, v66
	v_add_f32_e32 v66, v80, v66
	v_add_f32_e32 v66, v81, v66
	v_add_f32_e32 v192, v192, v66
	v_mfma_f32_32x32x16_bf16 v[2:17], v[110:113], v[70:73], v[2:17]
.LBB0_791:
	s_andn2_b64 vcc, exec, s[36:37]
	s_cbranch_vccnz .LBB0_780
	s_xor_b32 s0, s57, 1
	s_mulk_i32 s0, 0x2400
	v_add_u32_e32 v66, s0, v185
	s_xor_b32 s0, s57, 3
	s_mulk_i32 s0, 0x2400
	v_add_u32_e32 v67, s0, v185
	s_cmp_eq_u32 s59, 0
	s_cbranch_scc1 .Ldf_w0
	s_cmp_eq_u32 s57, 0
	s_cbranch_scc1 .Ldf_w2B
	s_waitcnt vmcnt(3)
	ds_write_b128 v66, v[102:105] offset:4096
	s_waitcnt vmcnt(2)
	ds_write_b128 v67, v[106:109] offset:4096
	s_branch .LBB0_780
.Ldf_w2B:
	s_waitcnt vmcnt(3)
	ds_write_b128 v66, v[214:217] offset:4096
	s_waitcnt vmcnt(2)
	ds_write_b128 v67, v[248:251] offset:4096
	s_branch .LBB0_780
.Ldf_w0:
	s_cmp_eq_u32 s57, 0
	s_cbranch_scc1 .Ldf_w0B
	s_waitcnt vmcnt(1)
	ds_write_b128 v66, v[102:105] offset:4096
	s_waitcnt vmcnt(0)
	ds_write_b128 v67, v[106:109] offset:4096
	s_branch .LBB0_780
.Ldf_w0B:
	s_waitcnt vmcnt(1)
	ds_write_b128 v66, v[214:217] offset:4096
	s_waitcnt vmcnt(0)
	ds_write_b128 v67, v[248:251] offset:4096
	s_branch .LBB0_780

; #define LAS __attribute__((address_space(3)))
; __device__ __forceinline__ int lt_tid(int wv) { int ln; asm volatile("v_mbcnt_lo_u32_b32 %0, -1, 0\n\tv_mbcnt_hi_u32_b32 %0, -1, %0" : "=v"(ln)); return (wv << 6) | ln; }
;     ...
;     const int tid = lt_tid(wvid), lane = tid & 63, wave = __builtin_amdgcn_readfirstlane(tid >> 6), l31 = lane & 31, hi = lane >> 5;
;     const bf16_t* U = (const bf16_t*)(ws + WS_U); const bf16_t* VT = (const bf16_t*)(ws + WS_VTA); bf16_t* MIX = (bf16_t*)(ws + WS_MIX);
;     unsigned* qhead = (unsigned*)(ws + WS_CTL) + CW_DQ + (qslot * 4 + 2 + l) * 64;
;     LAS float* btab = (LAS float*)lds;
;     LAS int* ucur = (LAS int*)(lds + 8 * 132 * 4);
;     LAS unsigned char* KV = lds + 8192;
;     constexpr float LOG2E = 1.4426950408889634f;
;     __syncthreads();
;     const float c2 = 0.125f * LOG2E;
;     for (int i = tid; i < 4 * 130; i += NTHR) { const int h = i / 130, n = i % 130;
.LBB0_795:
	s_waitcnt vmcnt(0)
	v_mov_b32_e32 v214, 0xbc800000
	v_mov_b32_e32 v215, 0x3c800000
	v_mov_b32_e32 v216, 1
	v_mov_b32_e32 v217, 0x2000
	v_mov_b32_e32 v249, 0x3a27c5ac
	v_mov_b32_e32 v250, 0x260
	v_mov_b32_e32 v251, 0x1010
	v_mov_b32_e32 v205, 0x100f
	s_mov_b32 s0, s65
	s_waitcnt lgkmcnt(0)
	s_barrier
	s_mov_b64 s[0:1], s[66:67]
	v_mbcnt_lo_u32_b32 v6, -1, 0
	v_mbcnt_hi_u32_b32 v6, -1, v6
	s_movk_i32 s2, 0x208
	v_or_b32_e32 v2, s75, v6
	v_cmp_gt_i32_e32 vcc, s2, v2
	v_readfirstlane_b32 s24, v2
	s_barrier
	s_and_saveexec_b64 s[2:3], vcc
	v_readlane_b32 s6, v255, 14
	s_mov_b32 s40, s6
	v_readlane_b32 s7, v255, 15
	s_cbranch_execz .LBB0_802
	v_lshl_add_u32 v3, v2, 2, 0
	s_mov_b64 s[4:5], 0
	v_mov_b32_e32 v0, v2
	s_branch .LBB0_799
